# baseline (speedup 1.0000x reference)
_Z11gemm_kernelILi128ELi192ELi1EEv8GemmArgs:
	s_load_dwordx2 s[4:5], s[0:1], 0x38
	s_load_dwordx2 s[22:23], s[0:1], 0x48
	s_load_dwordx2 s[24:25], s[0:1], 0x0
	s_load_dwordx2 s[26:27], s[0:1], 0x98
	s_addk_i32 s2, 0xe0
	s_mov_b32 s3, 0
	s_lshl_b64 s[6:7], s[2:3], 2
	s_waitcnt lgkmcnt(0)
	s_add_u32 s4, s4, s6
	s_addc_u32 s5, s5, s7
	s_load_dword s8, s[4:5], 0x0
	s_waitcnt lgkmcnt(0)
	s_cmp_lt_i32 s8, 0
	s_cbranch_scc1 .LBB3_4
	s_mov_b64 s[6:7], s[22:23]
	s_mov_b64 s[4:5], s[24:25]
	v_lshlrev_b32_e32 v64, 4, v0
	v_and_b32_e32 v1, 32, v0
	v_bitop3_b32 v1, v64, v1, 48 bitop3:0x6c
	s_and_b32 s2, s8, 0xffff
	v_bfe_u32 v4, v0, 2, 4
	v_lshrrev_b32_e32 v2, 1, v0
	v_lshrrev_b32_e32 v1, 1, v1
	v_lshrrev_b32_e32 v6, 3, v0
	v_and_or_b32 v1, v2, 32, v1
	v_add_u32_e32 v5, s2, v4
	v_and_b32_e32 v7, 48, v6
	s_movk_i32 s10, 0x70
	v_add_lshl_u32 v22, v5, v7, 12
	v_mov_b32_e32 v23, 0
	v_lshlrev_b32_e32 v44, 1, v1
	v_bitop3_b32 v1, v6, s10, 64 bitop3:0xc8
	s_waitcnt lgkmcnt(0)
	v_lshl_add_u64 v[2:3], s[4:5], 0, v[22:23]
	v_mov_b32_e32 v45, v23
	v_add_lshl_u32 v48, v5, v1, 12
	v_mov_b32_e32 v49, v23
	s_lshr_b32 s10, s8, 24
	s_bfe_u32 s9, s8, 0x80010
	v_lshl_add_u64 v[46:47], v[2:3], 0, v[44:45]
	v_lshl_add_u64 v[2:3], s[4:5], 0, v[48:49]
	s_mulk_i32 s10, 0x300
	v_lshl_add_u64 v[50:51], v[2:3], 0, v[44:45]
	s_mul_i32 s8, s9, 0xc0
	v_or_b32_e32 v2, s10, v4
	v_add_u32_e32 v4, s8, v2
	v_or_b32_e32 v2, v4, v7
	v_lshlrev_b32_e32 v52, 12, v2
	v_mov_b32_e32 v53, v23
	v_lshl_add_u64 v[2:3], s[6:7], 0, v[52:53]
	v_add_lshl_u32 v56, v4, v1, 12
	v_mov_b32_e32 v57, v23
	v_lshl_add_u64 v[54:55], v[2:3], 0, v[44:45]
	v_lshl_add_u64 v[2:3], s[6:7], 0, v[56:57]
	v_add_u32_e32 v60, 0x80000, v52
	v_mov_b32_e32 v61, v23
	v_lshl_add_u64 v[58:59], v[2:3], 0, v[44:45]
	v_lshl_add_u64 v[2:3], s[6:7], 0, v[60:61]
	v_lshl_add_u64 v[62:63], v[2:3], 0, v[44:45]
	v_readfirstlane_b32 s16, v0
	s_mov_b64 s[0:1], s[26:27]
	s_lshr_b32 s16, s16, 6
	s_lshl_b32 s16, s16, 10
	v_bfe_u32 v1, v0, 6, 2
	v_lshrrev_b32_e32 v80, 2, v0
	s_add_u32 m0, s16, 0
	s_nop 0
	global_load_lds_dwordx4 v[46:47], off
	s_add_u32 m0, s16, 8192
	s_nop 0
	global_load_lds_dwordx4 v[50:51], off
	s_add_u32 m0, s16, 16384
	s_nop 0
	global_load_lds_dwordx4 v[54:55], off
	s_add_u32 m0, s16, 24576
	s_nop 0
	global_load_lds_dwordx4 v[58:59], off
	s_add_u32 m0, s16, 32768
	s_nop 0
	global_load_lds_dwordx4 v[62:63], off
	s_add_u32 m0, s16, 40832
	s_nop 0
	global_load_lds_dwordx4 v[46:47], off offset:128
	s_add_u32 m0, s16, 49024
	s_nop 0
	global_load_lds_dwordx4 v[50:51], off offset:128
	s_add_u32 m0, s16, 57216
	s_nop 0
	global_load_lds_dwordx4 v[54:55], off offset:128
	s_add_u32 m0, s16, 65408
	s_nop 0
	global_load_lds_dwordx4 v[58:59], off offset:128
	s_add_u32 m0, s16, 73600
	s_nop 0
	global_load_lds_dwordx4 v[62:63], off offset:128
	s_mov_b32 s17, 0
	s_mov_b32 s18, 0xa000
	s_mov_b32 s19, 0x14000
	v_lshlrev_b32_e32 v25, 6, v0
	v_lshlrev_b32_e32 v27, 2, v0
	v_and_b32_e32 v24, 48, v0
	v_and_b32_e32 v25, 0x3c0, v25
	v_and_b32_e32 v27, 32, v27
	v_or_b32_e32 v26, v25, v24
	v_bitop3_b32 v87, v25, v27, v24 bitop3:0x36
	v_or_b32_e32 v24, v44, v60
	v_mov_b32_e32 v25, v23
	v_lshl_add_u64 v[24:25], s[6:7], 0, v[24:25]
	s_mov_b64 s[10:11], 0x100
	v_lshl_add_u64 v[70:71], v[24:25], 0, s[10:11]
	v_or_b32_e32 v24, v56, v44
	v_mov_b32_e32 v25, v23
	v_lshl_add_u64 v[24:25], s[6:7], 0, v[24:25]
	v_lshl_add_u64 v[72:73], v[24:25], 0, s[10:11]
	v_or_b32_e32 v24, v52, v44
	v_mov_b32_e32 v25, v23
	v_lshl_add_u64 v[24:25], s[6:7], 0, v[24:25]
	v_lshl_add_u64 v[74:75], v[24:25], 0, s[10:11]
	v_or_b32_e32 v24, v48, v44
	v_mov_b32_e32 v25, v23
	v_lshl_add_u64 v[24:25], s[4:5], 0, v[24:25]
	v_or_b32_e32 v22, v22, v44
	v_and_b32_e32 v81, 64, v80
	v_mul_u32_u24_e32 v86, 0x1800, v1
	v_lshl_add_u64 v[76:77], v[24:25], 0, s[10:11]
	v_lshl_add_u64 v[24:25], s[4:5], 0, v[22:23]
	v_bitop3_b32 v82, v26, v86, v27 bitop3:0xde
	v_lshlrev_b32_e32 v88, 7, v81
	v_lshl_add_u64 v[78:79], v[24:25], 0, s[10:11]
	s_mov_b64 s[4:5], 0
	v_mov_b32_e32 v22, v23
	v_mov_b32_e32 v24, v23
	v_mov_b32_e32 v25, v23
	v_mov_b32_e32 v50, v23
	v_mov_b32_e32 v51, v23
	v_mov_b32_e32 v52, v23
	v_mov_b32_e32 v54, v23
	v_mov_b32_e32 v55, v23
	v_mov_b32_e32 v56, v23
	v_mov_b32_e32 v58, v23
	v_mov_b32_e32 v59, v23
	v_mov_b32_e32 v60, v23
	v_mov_b32_e32 v66, v23
	v_mov_b32_e32 v67, v23
	v_mov_b32_e32 v68, v23
	v_mov_b32_e32 v69, v23
	v_mov_b32_e32 v62, v23
	v_mov_b32_e32 v63, v23
	v_mov_b32_e32 v64, v23
	v_mov_b32_e32 v65, v23
	v_mov_b32_e32 v42, v23
	v_mov_b32_e32 v43, v23
	v_mov_b32_e32 v44, v23
	v_mov_b32_e32 v46, v23
	v_mov_b32_e32 v47, v23
	v_mov_b32_e32 v48, v23
	v_mov_b32_e32 v30, v23
	v_mov_b32_e32 v31, v23
	v_mov_b32_e32 v32, v23
	v_mov_b32_e32 v33, v23
	v_mov_b32_e32 v34, v23
	v_mov_b32_e32 v35, v23
	v_mov_b32_e32 v36, v23
	v_mov_b32_e32 v37, v23
	v_mov_b32_e32 v38, v23
	v_mov_b32_e32 v39, v23
	v_mov_b32_e32 v40, v23
	v_mov_b32_e32 v41, v23
	v_mov_b32_e32 v26, v23
	v_mov_b32_e32 v27, v23
	v_mov_b32_e32 v28, v23
	v_mov_b32_e32 v29, v23
	s_waitcnt vmcnt(5) lgkmcnt(0)
	s_barrier
